# v71 + P3: waves 4-7 run each ticket's 12 weight-conversion items before its dilated-attention unit (waves 0-3 after), to overlap HBM streaming with attention compute on every SIMD
# baseline (speedup 1.0000x reference)
.LBB0_321:
	s_or_b64 exec, exec, s[2:3]
	s_add_u32 s6, s0, 0x8000
	s_addc_u32 s7, s1, 0
	s_lshl_b32 s5, s93, 8
	v_lshlrev_b32_e32 v170, 2, v176
	s_lshl_b32 s4, s93, 14
	s_add_i32 s25, s5, 0
	v_and_b32_e32 v0, 24, v177
	v_and_or_b32 v1, v179, 3, v170
	s_add_i32 s24, s4, 0
	s_add_i32 s25, s25, 0x21900
	v_lshlrev_b32_e32 v1, 6, v1
	v_and_or_b32 v2, v178, 32, s4
	v_add_u32_e32 v3, 0, v0
	s_movk_i32 s8, 0x6000
	v_add_u32_e32 v5, 8, v175
	v_add3_u32 v171, v3, v2, v1
	v_lshlrev_b32_e32 v2, 9, v176
	v_lshlrev_b32_e32 v3, 1, v173
	v_lshlrev_b32_e32 v6, 7, v5
	v_mad_i64_i32 v[150:151], s[20:21], v5, s8, 0
	v_add_u32_e32 v5, 16, v175
	s_add_u32 s26, s0, 0xa000000
	v_lshlrev_b32_e32 v146, 3, v176
	v_lshlrev_b32_e32 v180, 4, v176
	v_add3_u32 v176, s24, v2, v3
	v_and_b32_e32 v2, 56, v177
	v_lshlrev_b32_e32 v7, 7, v5
	v_mad_i64_i32 v[152:153], s[20:21], v5, s8, 0
	v_add_u32_e32 v5, 24, v175
	s_addc_u32 s27, s1, 0
	v_lshl_add_u32 v3, v2, 1, s24
	v_lshlrev_b32_e32 v4, 7, v175
	v_lshlrev_b32_e32 v8, 7, v5
	s_add_u32 s28, s0, 0x2000000
	s_mov_b32 s9, 0
	v_cmp_eq_u32_e64 s[2:3], 0, v172
	v_ashrrev_i32_e32 v147, 31, v146
	v_mov_b32_e32 v1, 0
	v_or_b32_e32 v178, 0xffffffa0, v173
	v_cmp_gt_u32_e64 s[4:5], 32, v172
	v_lshl_add_u32 v179, v173, 2, s25
	v_add_u32_e32 v181, 0x2000, v171
	v_mad_i64_i32 v[148:149], s[20:21], v175, s8, 0
	v_mad_i64_i32 v[154:155], s[20:21], v5, s8, 0
	s_addc_u32 s29, s1, 0
	v_sub_u32_e32 v175, 0x80, v170
	s_movk_i32 s30, 0x1e00
	v_lshlrev_b32_e32 v156, 1, v0
	s_add_i32 s31, s24, 0x400
	s_add_i32 s33, s24, 0x800
	s_add_i32 s34, s24, 0xc00
	s_add_i32 s35, s24, 0x1000
	s_add_i32 s36, s24, 0x1400
	s_add_i32 s37, s24, 0x1800
	s_add_i32 s38, s24, 0x1c00
	s_add_i32 s39, s24, 0x2400
	s_add_i32 s40, s24, 0x2800
	s_add_i32 s41, s24, 0x2c00
	s_add_i32 s42, s24, 0x3000
	s_add_i32 s43, s24, 0x3400
	s_add_i32 s44, s24, 0x3800
	s_add_i32 s45, s24, 0x3c00
	s_movk_i32 s46, 0xffe4
	s_movk_i32 s47, 0xffe5
	s_movk_i32 s48, 0xffe6
	s_movk_i32 s49, 0xffe7
	s_movk_i32 s50, 0xffec
	s_movk_i32 s51, 0xffed
	s_movk_i32 s52, 0xffee
	s_movk_i32 s53, 0xffef
	s_mov_b32 s54, 0xff800000
	s_movk_i32 s55, 0xffc4
	s_movk_i32 s56, 0xffc5
	s_movk_i32 s57, 0xffc6
	s_movk_i32 s58, 0xffc7
	s_movk_i32 s59, 0xffcc
	s_movk_i32 s60, 0xffcd
	s_movk_i32 s61, 0xffce
	s_movk_i32 s62, 0xffcf
	s_movk_i32 s63, 0xffd4
	s_movk_i32 s64, 0xffd5
	s_movk_i32 s65, 0xffd6
	s_movk_i32 s66, 0xffd7
	s_movk_i32 s67, 0xffdc
	s_movk_i32 s68, 0xffdd
	s_movk_i32 s69, 0xffde
	s_movk_i32 s70, 0xffdf
	s_movk_i32 s71, 0x7fff
	v_lshlrev_b32_e32 v158, 1, v2
	v_add_u32_e32 v177, v3, v4
	v_add_u32_e32 v182, v3, v6
	v_add_u32_e32 v183, v3, v7
	v_add_u32_e32 v184, v3, v8
	s_movk_i32 s72, 0x84
	s_mov_b32 s73, 0xc3e00000
	v_mov_b32_e32 v185, 0x81
	v_mov_b32_e32 v186, 0xa1
	v_mov_b32_e32 v187, 0xff800000
	v_mov_b32_e32 v188, 0x43e00000
	s_waitcnt vmcnt(0) lgkmcnt(0)
	s_barrier
	s_lshr_b32 s91, s93, 2
	s_branch .LBB0_324

.LBB0_328:
	s_or_b64 exec, exec, s[0:1]
	v_readfirstlane_b32 s22, v0
	s_cmpk_gt_u32 s22, 0xfff
	s_mov_b64 s[0:1], -1
	s_cbranch_scc1 .LBB0_323
	s_cmp_eq_u32 s91, 0
	s_cbranch_scc1 .Ldil_start
	s_mul_i32 s20, s22, 12
	s_mov_b32 s23, 0
	s_branch .Lcv3_entry
.Ldil_start:
	s_lshl_b32 s0, s22, 5
	s_and_b32 s8, s0, 0x1e0
	s_lshl_b32 s0, s22, 3
	s_and_b32 s75, s0, 0x6000
	s_lshr_b32 s76, s22, 4
	s_bfe_u32 s74, s22, 0x40004
	s_bfe_u32 s23, s22, 0x20008
	v_or_b32_e32 v0, s8, v173
	s_mul_i32 s0, s75, 0x1e00
	v_lshl_or_b32 v159, v0, 4, s74
	s_add_u32 s0, s16, s0
	s_addc_u32 s1, s17, 0
	v_mul_u32_u24_e32 v0, 0xf00, v159
	s_add_u32 s78, s0, 0x1200
	v_lshlrev_b32_e32 v0, 1, v0
	s_addc_u32 s79, s1, 0
	v_lshl_add_u64 v[2:3], s[0:1], 0, v[0:1]
	v_mov_b32_e32 v14, v1
	v_mov_b32_e32 v15, v1
	s_add_u32 s80, s0, 0x1800
	v_lshl_add_u64 v[160:161], v[146:147], 1, v[2:3]
	v_mov_b32_e32 v0, v1
	v_mov_b32_e32 v2, v1
	v_mov_b32_e32 v3, v1
	v_mov_b32_e32 v4, v1
	v_mov_b32_e32 v5, v1
	v_mov_b32_e32 v6, v1
	v_mov_b32_e32 v7, v1
	v_mov_b32_e32 v8, v1
	v_mov_b32_e32 v9, v1
	v_mov_b32_e32 v10, v1
	v_mov_b32_e32 v11, v1
	v_mov_b32_e32 v12, v1
	v_mov_b32_e32 v13, v1
	v_mov_b64_e32 v[32:33], v[14:15]
	s_addc_u32 s81, s1, 0
	s_lshl_b32 s77, s8, 4
	v_mov_b64_e32 v[30:31], v[12:13]
	v_mov_b64_e32 v[28:29], v[10:11]
	v_mov_b64_e32 v[26:27], v[8:9]
	v_mov_b64_e32 v[24:25], v[6:7]
	v_mov_b64_e32 v[22:23], v[4:5]
	v_mov_b64_e32 v[20:21], v[2:3]
	v_mov_b64_e32 v[18:19], v[0:1]
	v_mov_b64_e32 v[16:17], v[14:15]
	s_or_b32 s82, s77, s74
	s_mov_b32 s83, 0
	v_mov_b32_e32 v189, 0
	v_mov_b32_e32 v190, 0xff800000
	v_mov_b64_e32 v[14:15], v[12:13]
	v_mov_b64_e32 v[12:13], v[10:11]
	v_mov_b64_e32 v[10:11], v[8:9]
	v_mov_b64_e32 v[8:9], v[6:7]
	v_mov_b64_e32 v[6:7], v[4:5]
	v_mov_b64_e32 v[4:5], v[2:3]
	v_mov_b64_e32 v[2:3], v[0:1]
	s_branch .LBB0_331

.LBB0_357:
	s_waitcnt lgkmcnt(0)
	v_mov_b32_e32 v0, v189
	s_nop 1
	v_permlane32_swap_b32_e32 v189, v0
	s_and_saveexec_b64 s[0:1], s[4:5]
	v_add_f32_e32 v0, v189, v0
	ds_write_b32 v179, v0 offset:128
	s_or_b64 exec, exec, s[0:1]
	s_waitcnt lgkmcnt(0)
	v_add_u32_e32 v0, s25, v180
	ds_read_b128 v[34:37], v0 offset:128
	ds_read_b128 v[38:41], v0 offset:160
	s_or_b32 s0, s75, s77
	s_or_b32 s0, s0, s74
	s_mulk_i32 s0, 0x600
	s_waitcnt lgkmcnt(0)
	v_rcp_f32_e32 v42, v34
	v_rcp_f32_e32 v43, v35
	v_rcp_f32_e32 v44, v36
	v_rcp_f32_e32 v45, v37
	v_rcp_f32_e32 v46, v38
	ds_read_b128 v[34:37], v0 offset:192
	v_rcp_f32_e32 v47, v39
	v_rcp_f32_e32 v48, v40
	v_rcp_f32_e32 v49, v41
	ds_read_b128 v[38:41], v0 offset:224
	v_mul_f32_e32 v18, v18, v42
	s_waitcnt lgkmcnt(0)
	v_rcp_f32_e32 v0, v34
	v_rcp_f32_e32 v34, v35
	v_rcp_f32_e32 v35, v36
	v_rcp_f32_e32 v36, v37
	v_rcp_f32_e32 v37, v38
	v_rcp_f32_e32 v38, v39
	v_rcp_f32_e32 v39, v40
	v_rcp_f32_e32 v40, v41
	v_bfe_u32 v41, v18, 16, 1
	v_add3_u32 v18, v18, v41, s71
	v_mul_f32_e32 v2, v2, v42
	ds_write_b16_d16_hi v176, v18
	v_bfe_u32 v18, v2, 16, 1
	v_add3_u32 v2, v2, v18, s71
	ds_write_b16_d16_hi v176, v2 offset:64
	v_mul_f32_e32 v2, v19, v43
	v_bfe_u32 v18, v2, 16, 1
	v_add3_u32 v2, v2, v18, s71
	ds_write_b16_d16_hi v176, v2 offset:128
	v_mul_f32_e32 v2, v3, v43
	v_bfe_u32 v3, v2, 16, 1
	v_add3_u32 v2, v2, v3, s71
	ds_write_b16_d16_hi v176, v2 offset:192
	v_mul_f32_e32 v2, v20, v44
	v_bfe_u32 v3, v2, 16, 1
	v_add3_u32 v2, v2, v3, s71
	ds_write_b16_d16_hi v176, v2 offset:256
	v_mul_f32_e32 v2, v4, v44
	v_bfe_u32 v3, v2, 16, 1
	v_add3_u32 v2, v2, v3, s71
	ds_write_b16_d16_hi v176, v2 offset:320
	v_mul_f32_e32 v2, v21, v45
	v_bfe_u32 v3, v2, 16, 1
	v_add3_u32 v2, v2, v3, s71
	ds_write_b16_d16_hi v176, v2 offset:384
	v_mul_f32_e32 v2, v5, v45
	v_bfe_u32 v3, v2, 16, 1
	v_add3_u32 v2, v2, v3, s71
	ds_write_b16_d16_hi v176, v2 offset:448
	v_mul_f32_e32 v2, v22, v46
	v_bfe_u32 v3, v2, 16, 1
	v_add3_u32 v2, v2, v3, s71
	ds_write_b16_d16_hi v176, v2 offset:1024
	v_mul_f32_e32 v2, v6, v46
	v_bfe_u32 v3, v2, 16, 1
	v_add3_u32 v2, v2, v3, s71
	ds_write_b16_d16_hi v176, v2 offset:1088
	v_mul_f32_e32 v2, v23, v47
	v_bfe_u32 v3, v2, 16, 1
	v_add3_u32 v2, v2, v3, s71
	ds_write_b16_d16_hi v176, v2 offset:1152
	v_mul_f32_e32 v2, v7, v47
	v_bfe_u32 v3, v2, 16, 1
	v_add3_u32 v2, v2, v3, s71
	ds_write_b16_d16_hi v176, v2 offset:1216
	v_mul_f32_e32 v2, v24, v48
	v_bfe_u32 v3, v2, 16, 1
	v_add3_u32 v2, v2, v3, s71
	ds_write_b16_d16_hi v176, v2 offset:1280
	v_mul_f32_e32 v2, v8, v48
	v_bfe_u32 v3, v2, 16, 1
	v_add3_u32 v2, v2, v3, s71
	ds_write_b16_d16_hi v176, v2 offset:1344
	v_mul_f32_e32 v2, v25, v49
	v_bfe_u32 v3, v2, 16, 1
	v_add3_u32 v2, v2, v3, s71
	ds_write_b16_d16_hi v176, v2 offset:1408
	v_mul_f32_e32 v2, v9, v49
	v_bfe_u32 v3, v2, 16, 1
	v_add3_u32 v2, v2, v3, s71
	ds_write_b16_d16_hi v176, v2 offset:1472
	v_mul_f32_e32 v2, v26, v0
	v_bfe_u32 v3, v2, 16, 1
	v_add3_u32 v2, v2, v3, s71
	v_mul_f32_e32 v0, v10, v0
	ds_write_b16_d16_hi v176, v2 offset:2048
	v_bfe_u32 v2, v0, 16, 1
	v_add3_u32 v0, v0, v2, s71
	ds_write_b16_d16_hi v176, v0 offset:2112
	v_mul_f32_e32 v0, v27, v34
	v_bfe_u32 v2, v0, 16, 1
	v_add3_u32 v0, v0, v2, s71
	ds_write_b16_d16_hi v176, v0 offset:2176
	v_mul_f32_e32 v0, v11, v34
	v_bfe_u32 v2, v0, 16, 1
	v_add3_u32 v0, v0, v2, s71
	ds_write_b16_d16_hi v176, v0 offset:2240
	v_mul_f32_e32 v0, v28, v35
	v_bfe_u32 v2, v0, 16, 1
	v_add3_u32 v0, v0, v2, s71
	ds_write_b16_d16_hi v176, v0 offset:2304
	v_mul_f32_e32 v0, v12, v35
	v_bfe_u32 v2, v0, 16, 1
	v_add3_u32 v0, v0, v2, s71
	ds_write_b16_d16_hi v176, v0 offset:2368
	v_mul_f32_e32 v0, v29, v36
	v_bfe_u32 v2, v0, 16, 1
	v_add3_u32 v0, v0, v2, s71
	ds_write_b16_d16_hi v176, v0 offset:2432
	v_mul_f32_e32 v0, v13, v36
	v_bfe_u32 v2, v0, 16, 1
	v_add3_u32 v0, v0, v2, s71
	ds_write_b16_d16_hi v176, v0 offset:2496
	v_mul_f32_e32 v0, v30, v37
	v_bfe_u32 v2, v0, 16, 1
	v_add3_u32 v0, v0, v2, s71
	ds_write_b16_d16_hi v176, v0 offset:3072
	v_mul_f32_e32 v0, v14, v37
	v_bfe_u32 v2, v0, 16, 1
	v_add3_u32 v0, v0, v2, s71
	ds_write_b16_d16_hi v176, v0 offset:3136
	v_mul_f32_e32 v0, v31, v38
	v_bfe_u32 v2, v0, 16, 1
	v_add3_u32 v0, v0, v2, s71
	ds_write_b16_d16_hi v176, v0 offset:3200
	v_mul_f32_e32 v0, v15, v38
	v_bfe_u32 v2, v0, 16, 1
	v_add3_u32 v0, v0, v2, s71
	ds_write_b16_d16_hi v176, v0 offset:3264
	v_mul_f32_e32 v0, v32, v39
	v_bfe_u32 v2, v0, 16, 1
	v_add3_u32 v0, v0, v2, s71
	ds_write_b16_d16_hi v176, v0 offset:3328
	v_mul_f32_e32 v0, v16, v39
	v_bfe_u32 v2, v0, 16, 1
	v_add3_u32 v0, v0, v2, s71
	ds_write_b16_d16_hi v176, v0 offset:3392
	v_mul_f32_e32 v0, v33, v40
	v_bfe_u32 v2, v0, 16, 1
	v_add3_u32 v0, v0, v2, s71
	ds_write_b16_d16_hi v176, v0 offset:3456
	v_mul_f32_e32 v0, v17, v40
	v_bfe_u32 v2, v0, 16, 1
	v_add3_u32 v0, v0, v2, s71
	ds_write_b16_d16_hi v176, v0 offset:3520
	s_add_u32 s0, s18, s0
	s_waitcnt lgkmcnt(0)
	s_addc_u32 s1, s19, 0
	s_lshl_b32 s8, s23, 7
	ds_read_b128 v[2:5], v177
	ds_read_b128 v[6:9], v182
	s_add_u32 s0, s0, s8
	s_addc_u32 s1, s1, 0
	v_mov_b32_e32 v159, v1
	v_lshl_add_u64 v[14:15], s[0:1], 0, v[158:159]
	v_lshl_add_u64 v[10:11], v[14:15], 0, v[148:149]
	s_waitcnt lgkmcnt(0)
	global_store_dwordx4 v[10:11], v[2:5], off offset:1024
	ds_read_b128 v[2:5], v183
	ds_read_b128 v[10:13], v184
	v_lshl_add_u64 v[16:17], v[14:15], 0, v[150:151]
	global_store_dwordx4 v[16:17], v[6:9], off offset:1024
	s_mul_i32 s20, s22, 12
	s_mul_i32 s21, s22, 24
	v_lshl_add_u64 v[6:7], v[14:15], 0, v[152:153]
	s_waitcnt lgkmcnt(0)
	global_store_dwordx4 v[6:7], v[2:5], off offset:1024
	s_mulk_i32 s22, 0x180
	s_mov_b32 s23, 0
	v_lshl_add_u64 v[2:3], v[14:15], 0, v[154:155]
	global_store_dwordx4 v[2:3], v[10:13], off offset:1024
	s_waitcnt lgkmcnt(0)
	s_waitcnt vmcnt(0) lgkmcnt(0)
	v_readlane_b32 s88, v254, 9
	s_cmp_lg_u32 s91, 0
	s_cbranch_scc1 .LBB0_322
.Lcv3_entry:
	v_and_b32_e32 v234, 31, v172
	v_lshrrev_b32_e32 v239, 5, v172
	v_lshlrev_b32_e32 v235, 2, v234
	v_add_u32_e32 v235, s24, v235
	v_mul_u32_u24_e32 v240, 0x1080, v239
	v_add_u32_e32 v236, v235, v240
	v_mul_u32_u24_e32 v240, 0x84, v239
	v_add_u32_e32 v235, v235, v240
	s_cmpk_gt_u32 s20, 0x7fff
	s_cbranch_scc1 .Lcv3_w2_a
	s_lshr_b32 s84, s20, 10
	s_mov_b32 s85, 0
	s_lshl_b64 s[86:87], s[84:85], 23
	s_add_u32 s86, s12, s86
	s_addc_u32 s87, s13, s87
	s_lshl_b64 s[84:85], s[84:85], 21
	s_add_u32 s84, s28, s84
	s_addc_u32 s85, s29, s85
	s_and_b32 s80, s20, 0x3c0
	s_lshl_b32 s83, s20, 5
	s_and_b32 s83, s83, 0x7e0
	s_mov_b32 s89, 13
	s_branch .Lcv3_cm_a

.Lcv3_noissue:
	ds_write2_b32 v235, v8, v9 offset0:0 offset1:66
	ds_write2_b32 v235, v10, v11 offset0:132 offset1:198
	v_add_u32_e32 v240, 0x400, v235
	ds_write2_b32 v240, v12, v13 offset0:8 offset1:74
	ds_write2_b32 v240, v14, v15 offset0:140 offset1:206
	v_add_u32_e32 v240, 0x800, v235
	ds_write2_b32 v240, v16, v17 offset0:16 offset1:82
	ds_write2_b32 v240, v18, v19 offset0:148 offset1:214
	v_add_u32_e32 v240, 0xc00, v235
	ds_write2_b32 v240, v20, v21 offset0:24 offset1:90
	ds_write2_b32 v240, v22, v23 offset0:156 offset1:222
	v_add_u32_e32 v240, 0x1000, v235
	ds_write2_b32 v240, v24, v25 offset0:32 offset1:98
	ds_write2_b32 v240, v26, v27 offset0:164 offset1:230
	v_add_u32_e32 v240, 0x1400, v235
	ds_write2_b32 v240, v28, v29 offset0:40 offset1:106
	ds_write2_b32 v240, v30, v31 offset0:172 offset1:238
	v_add_u32_e32 v240, 0x1800, v235
	ds_write2_b32 v240, v32, v33 offset0:48 offset1:114
	ds_write2_b32 v240, v34, v35 offset0:180 offset1:246
	v_add_u32_e32 v240, 0x1c00, v235
	ds_write2_b32 v240, v36, v37 offset0:56 offset1:122
	ds_write2_b32 v240, v38, v39 offset0:188 offset1:254
	s_waitcnt lgkmcnt(0)
	ds_read2_b32 v[8:9], v236 offset0:0 offset1:33
	ds_read2_b32 v[10:11], v236 offset0:66 offset1:99
	ds_read2_b32 v[12:13], v236 offset0:132 offset1:165
	ds_read2_b32 v[14:15], v236 offset0:198 offset1:231
	v_add_u32_e32 v240, 0x400, v236
	ds_read2_b32 v[16:17], v240 offset0:8 offset1:41
	ds_read2_b32 v[18:19], v240 offset0:74 offset1:107
	ds_read2_b32 v[20:21], v240 offset0:140 offset1:173
	ds_read2_b32 v[22:23], v240 offset0:206 offset1:239
	v_add_u32_e32 v240, 0x800, v236
	ds_read2_b32 v[24:25], v240 offset0:16 offset1:49
	ds_read2_b32 v[26:27], v240 offset0:82 offset1:115
	ds_read2_b32 v[28:29], v240 offset0:148 offset1:181
	ds_read2_b32 v[30:31], v240 offset0:214 offset1:247
	v_add_u32_e32 v240, 0xc00, v236
	ds_read2_b32 v[32:33], v240 offset0:24 offset1:57
	ds_read2_b32 v[34:35], v240 offset0:90 offset1:123
	ds_read2_b32 v[36:37], v240 offset0:156 offset1:189
	ds_read2_b32 v[38:39], v240 offset0:222 offset1:255
	s_waitcnt lgkmcnt(14)
	v_med3_f32 v8, v8, s73, v188
	v_med3_f32 v9, v9, s73, v188
	v_med3_f32 v10, v10, s73, v188
	v_med3_f32 v11, v11, s73, v188
	v_cvt_pk_fp8_f32 v224, v8, v9
	v_cvt_pk_fp8_f32 v224, v10, v11 op_sel:[0,0,1]
	s_waitcnt lgkmcnt(12)
	v_med3_f32 v12, v12, s73, v188
	v_med3_f32 v13, v13, s73, v188
	v_med3_f32 v14, v14, s73, v188
	v_med3_f32 v15, v15, s73, v188
	v_cvt_pk_fp8_f32 v225, v12, v13
	v_cvt_pk_fp8_f32 v225, v14, v15 op_sel:[0,0,1]
	s_waitcnt lgkmcnt(10)
	v_med3_f32 v16, v16, s73, v188
	v_med3_f32 v17, v17, s73, v188
	v_med3_f32 v18, v18, s73, v188
	v_med3_f32 v19, v19, s73, v188
	v_cvt_pk_fp8_f32 v226, v16, v17
	v_cvt_pk_fp8_f32 v226, v18, v19 op_sel:[0,0,1]
	s_waitcnt lgkmcnt(8)
	v_med3_f32 v20, v20, s73, v188
	v_med3_f32 v21, v21, s73, v188
	v_med3_f32 v22, v22, s73, v188
	v_med3_f32 v23, v23, s73, v188
	v_cvt_pk_fp8_f32 v227, v20, v21
	v_cvt_pk_fp8_f32 v227, v22, v23 op_sel:[0,0,1]
	s_waitcnt lgkmcnt(6)
	v_med3_f32 v24, v24, s73, v188
	v_med3_f32 v25, v25, s73, v188
	v_med3_f32 v26, v26, s73, v188
	v_med3_f32 v27, v27, s73, v188
	v_cvt_pk_fp8_f32 v228, v24, v25
	v_cvt_pk_fp8_f32 v228, v26, v27 op_sel:[0,0,1]
	s_waitcnt lgkmcnt(4)
	v_med3_f32 v28, v28, s73, v188
	v_med3_f32 v29, v29, s73, v188
	v_med3_f32 v30, v30, s73, v188
	v_med3_f32 v31, v31, s73, v188
	v_cvt_pk_fp8_f32 v229, v28, v29
	v_cvt_pk_fp8_f32 v229, v30, v31 op_sel:[0,0,1]
	s_waitcnt lgkmcnt(2)
	v_med3_f32 v32, v32, s73, v188
	v_med3_f32 v33, v33, s73, v188
	v_med3_f32 v34, v34, s73, v188
	v_med3_f32 v35, v35, s73, v188
	v_cvt_pk_fp8_f32 v230, v32, v33
	v_cvt_pk_fp8_f32 v230, v34, v35 op_sel:[0,0,1]
	s_waitcnt lgkmcnt(0)
	v_med3_f32 v36, v36, s73, v188
	v_med3_f32 v37, v37, s73, v188
	v_med3_f32 v38, v38, s73, v188
	v_med3_f32 v39, v39, s73, v188
	v_cvt_pk_fp8_f32 v231, v36, v37
	v_cvt_pk_fp8_f32 v231, v38, v39 op_sel:[0,0,1]
	global_store_dwordx4 v238, v[224:227], s[98:99]
	global_store_dwordx4 v238, v[228:231], s[98:99] offset:16
	s_cmp_eq_u32 s23, 24
	s_cbranch_scc0 .Lcv3_top
	s_cmp_lg_u32 s91, 0
	s_cbranch_scc1 .Ldil_start
	s_branch .LBB0_322
